# v42 + GEMM prologue waits relaxed to vmcnt(10) (only the stages the first phase reads are waited at phase start)
# speedup vs baseline: 1.0074x; 1.0074x over previous
.LBB0_343:
	s_add_u32 s20, s4, 0x5900000
	s_addc_u32 s21, s5, 0
	s_add_i32 s22, s12, 0x18000
	s_or_b32 s4, s39, 0x80
	s_mov_b32 s10, s74
	s_mov_b32 s11, s75
	s_mov_b32 m0, s22
	s_add_i32 s2, s12, 0x1a000
	s_waitcnt vmcnt(4)
	s_barrier
	buffer_load_dwordx4 v96, s[8:11], s4 offen lds
	s_mov_b32 m0, s2
	s_add_i32 s23, s12, 0x8000
	buffer_load_dwordx4 v130, s[8:11], s4 offen lds
	s_mov_b32 m0, s23
	v_readlane_b32 s4, v253, 28
	s_add_i32 s24, s12, 0xa000
	s_add_i32 s25, s12, 0x1c000
	s_add_i32 s26, s12, 0x1e000
	v_and_b32_e32 v1, 15, v0
	v_bfe_u32 v2, v0, 1, 1
	buffer_load_dwordx4 v96, s[72:75], s4 offen lds
	s_mov_b32 m0, s24
	v_and_b32_e32 v3, 4, v0
	buffer_load_dwordx4 v130, s[72:75], s4 offen lds
	s_or_b32 s4, s39, 0x40080
	s_mov_b32 m0, s25
	v_lshrrev_b32_e32 v0, 3, v0
	buffer_load_dwordx4 v96, s[8:11], s4 offen lds
	s_mov_b32 m0, s26
	v_and_b32_e32 v0, 6, v0
	buffer_load_dwordx4 v130, s[8:11], s4 offen lds
	s_lshl_b32 s4, s6, 5
	v_lshlrev_b32_e32 v4, 7, v1
	v_bitop3_b32 v0, v2, v0, v3 bitop3:0x36
	s_and_b32 s4, s4, 0x60
	v_lshl_or_b32 v4, s7, 13, v4
	v_lshlrev_b32_e32 v0, 4, v0
	v_or_b32_e32 v1, s4, v1
	s_waitcnt vmcnt(10)
	v_or_b32_e32 v2, v0, v4
	v_lshlrev_b32_e32 v1, 7, v1
	v_bitop3_b32 v3, v0, 16, v4 bitop3:0x36
	v_or_b32_e32 v131, v1, v0
	v_bitop3_b32 v132, v1, 16, v0 bitop3:0x36
	s_add_i32 s27, s12, 0xc000
	s_add_i32 s28, s12, 0xe000
	s_mov_b32 s29, 0
	v_add_u32_e32 v133, 0, v2
	v_add_u32_e32 v134, 0, v3
	v_readlane_b32 s37, v253, 25
	v_readlane_b32 s10, v253, 27
	s_barrier
	s_waitcnt vmcnt(10)

.LBB0_480:
	s_add_u32 s23, s12, 0x13100000
	s_addc_u32 s24, s13, 0
	s_add_i32 s25, s15, 0x18000
	s_mov_b32 s10, s74
	s_mov_b32 s11, s75
	s_mov_b32 m0, s25
	v_readlane_b32 s6, v253, 35
	s_add_i32 s26, s15, 0x1a000
	s_waitcnt vmcnt(4)
	s_barrier
	s_add_i32 s27, s15, 0x8000
	s_add_i32 s28, s15, 0xa000
	s_nop 0
	buffer_load_dwordx4 v130, s[8:11], s6 offen lds
	s_mov_b32 m0, s26
	s_add_i32 s29, s15, 0x1c000
	buffer_load_dwordx4 v132, s[8:11], s6 offen lds
	s_mov_b32 m0, s27
	v_readlane_b32 s6, v253, 36
	s_add_i32 s30, s15, 0x1e000
	v_and_b32_e32 v1, 15, v0
	v_and_b32_e32 v2, 48, v0
	v_lshlrev_b32_e32 v0, 2, v0
	v_lshl_or_b32 v1, v1, 6, v2
	buffer_load_dwordx4 v96, s[72:75], s6 offen lds
	s_mov_b32 m0, s28
	s_lshl_b32 s5, s5, 13
	buffer_load_dwordx4 v131, s[72:75], s6 offen lds
	s_mov_b32 m0, s29
	v_readlane_b32 s6, v253, 37
	v_and_b32_e32 v0, 32, v0
	v_bitop3_b32 v2, v1, s5, v0 bitop3:0xde
	s_lshl_b32 s4, s4, 12
	s_add_i32 s5, 0, 0x10000
	s_and_b32 s4, s4, 0x3000
	buffer_load_dwordx4 v130, s[8:11], s6 offen lds
	s_mov_b32 m0, s30
	v_xad_u32 v0, v1, v0, s5
	buffer_load_dwordx4 v132, s[8:11], s6 offen lds
	s_waitcnt vmcnt(10)
	s_add_i32 s31, s15, 0xc000
	s_add_i32 s34, s15, 0xe000
	s_mov_b32 s35, 0
	v_add_u32_e32 v133, s4, v0
	v_add_u32_e32 v134, 0, v2
	v_readlane_b32 s40, v253, 33
	v_readlane_b32 s41, v253, 34
	v_readlane_b32 s10, v253, 51
	v_readlane_b32 s11, v253, 49
	s_barrier
	s_waitcnt vmcnt(10)

.LBB0_1351:
	s_add_u32 s28, s4, 0x5900000
	s_addc_u32 s29, s5, 0
	s_add_i32 s30, s2, 0x18000
	s_or_b32 s4, s46, 0x80
	s_mov_b32 s10, s74
	s_mov_b32 s11, s75
	s_mov_b32 m0, s30
	s_add_i32 s31, s2, 0x1a000
	s_waitcnt vmcnt(4)
	s_barrier
	buffer_load_dwordx4 v132, s[8:11], s4 offen lds
	s_mov_b32 m0, s31
	s_add_i32 s34, s2, 0x8000
	buffer_load_dwordx4 v134, s[8:11], s4 offen lds
	s_or_b32 s4, s45, 0x80
	s_mov_b32 m0, s34
	s_add_i32 s35, s2, 0xa000
	buffer_load_dwordx4 v131, s[72:75], s4 offen lds
	s_mov_b32 m0, s35
	s_add_i32 s36, s2, 0x1c000
	buffer_load_dwordx4 v133, s[72:75], s4 offen lds
	s_or_b32 s4, s46, 0x20080
	s_mov_b32 m0, s36
	s_add_i32 s37, s2, 0x1e000
	buffer_load_dwordx4 v132, s[8:11], s4 offen lds
	s_mov_b32 m0, s37
	v_and_b32_e32 v1, 15, v0
	buffer_load_dwordx4 v134, s[8:11], s4 offen lds
	v_and_b32_e32 v2, 48, v0
	v_lshlrev_b32_e32 v0, 2, v0
	v_lshl_or_b32 v1, v1, 6, v2
	s_lshl_b32 s4, s15, 13
	v_and_b32_e32 v0, 32, v0
	v_bitop3_b32 v2, v1, s4, v0 bitop3:0xde
	s_lshl_b32 s4, s16, 12
	s_add_i32 s5, 0, 0x10000
	s_waitcnt vmcnt(10)
	s_and_b32 s4, s4, 0x3000
	v_xad_u32 v0, v1, v0, s5
	s_add_i32 s38, s2, 0xc000
	s_add_i32 s39, s2, 0xe000
	s_mov_b32 s40, 0
	v_add_u32_e32 v135, s4, v0
	v_add_u32_e32 v136, 0, v2
	s_barrier
	s_waitcnt vmcnt(10)

.LBB0_1420:
	s_lshl_b32 s0, s66, 13
	s_add_u32 s12, s14, 0x1d300000
	s_addc_u32 s13, s15, 0
	s_add_u32 s14, s14, 0x5900000
	s_addc_u32 s15, s15, 0
	s_lshl_b64 s[10:11], s[0:1], 2
	s_add_u32 s16, s4, s10
	s_addc_u32 s17, s5, s11
	s_add_i32 s0, s27, 0x18000
	s_or_b32 s4, s47, 0x80
	s_mov_b32 s10, s74
	s_mov_b32 s11, s75
	s_mov_b32 m0, s0
	s_add_i32 s37, s27, 0x1a000
	s_waitcnt vmcnt(4)
	s_barrier
	buffer_load_dwordx4 v96, s[8:11], s4 offen lds
	s_mov_b32 m0, s37
	s_add_i32 s38, s27, 0x8000
	buffer_load_dwordx4 v218, s[8:11], s4 offen lds
	s_or_b32 s4, s46, 0x80
	s_mov_b32 m0, s38
	s_add_i32 s39, s27, 0xa000
	buffer_load_dwordx4 v96, s[72:75], s4 offen lds
	s_mov_b32 m0, s39
	s_add_i32 s40, s27, 0x1c000
	buffer_load_dwordx4 v218, s[72:75], s4 offen lds
	s_or_b32 s4, s47, 0x40080
	s_mov_b32 m0, s40
	s_add_i32 s41, s27, 0x1e000
	buffer_load_dwordx4 v96, s[8:11], s4 offen lds
	s_mov_b32 m0, s41
	v_and_b32_e32 v1, 15, v0
	buffer_load_dwordx4 v218, s[8:11], s4 offen lds
	v_bfe_u32 v2, v0, 1, 1
	v_and_b32_e32 v3, 4, v0
	v_lshrrev_b32_e32 v0, 3, v0
	v_and_b32_e32 v0, 6, v0
	s_lshl_b32 s4, s20, 5
	v_lshlrev_b32_e32 v4, 7, v1
	v_bitop3_b32 v0, v2, v0, v3 bitop3:0x36
	s_and_b32 s4, s4, 0x60
	v_lshl_or_b32 v4, s19, 13, v4
	v_lshlrev_b32_e32 v0, 4, v0
	v_or_b32_e32 v1, s4, v1
	s_waitcnt vmcnt(10)
	v_or_b32_e32 v2, v0, v4
	v_lshlrev_b32_e32 v1, 7, v1
	v_bitop3_b32 v3, v0, 16, v4 bitop3:0x36
	v_or_b32_e32 v228, v1, v0
	v_bitop3_b32 v229, v1, 16, v0 bitop3:0x36
	s_add_i32 s42, s27, 0xc000
	s_add_i32 s43, s27, 0xe000
	s_mov_b32 s44, 0
	v_add_u32_e32 v230, 0, v2
	v_add_u32_e32 v231, 0, v3
	s_barrier

.LBB0_1489:
	s_add_i32 s38, s28, 0x18000
	s_or_b32 s20, s51, 0x80
	s_mov_b32 s10, s74
	s_mov_b32 s11, s75
	s_mov_b32 m0, s38
	s_add_i32 s39, s28, 0x1a000
	s_waitcnt vmcnt(4)
	s_barrier
	buffer_load_dwordx4 v150, s[8:11], s20 offen lds
	s_mov_b32 m0, s39
	s_add_i32 s40, s28, 0x8000
	buffer_load_dwordx4 v152, s[8:11], s20 offen lds
	s_or_b32 s20, s50, 0x80
	s_mov_b32 m0, s40
	s_add_i32 s41, s28, 0xa000
	buffer_load_dwordx4 v149, s[72:75], s20 offen lds
	s_mov_b32 m0, s41
	s_add_i32 s42, s28, 0x1c000
	buffer_load_dwordx4 v151, s[72:75], s20 offen lds
	s_or_b32 s20, s51, 0x80080
	s_mov_b32 m0, s42
	s_add_i32 s43, s28, 0x1e000
	buffer_load_dwordx4 v150, s[8:11], s20 offen lds
	s_mov_b32 m0, s43
	v_and_b32_e32 v1, 15, v0
	buffer_load_dwordx4 v152, s[8:11], s20 offen lds
	v_and_b32_e32 v2, 48, v0
	v_lshlrev_b32_e32 v0, 2, v0
	v_lshl_or_b32 v1, v1, 6, v2
	s_lshl_b32 s4, s4, 13
	v_and_b32_e32 v0, 32, v0
	v_bitop3_b32 v2, v1, s4, v0 bitop3:0xde
	s_lshl_b32 s4, s5, 12
	s_add_i32 s5, 0, 0x10000
	s_waitcnt vmcnt(10)
	s_and_b32 s4, s4, 0x3000
	v_xad_u32 v0, v1, v0, s5
	s_add_i32 s44, s28, 0xc000
	s_add_i32 s45, s28, 0xe000
	s_mov_b32 s46, 0
	v_add_u32_e32 v153, s4, v0
	v_add_u32_e32 v154, 0, v2
	s_barrier

.LBB0_1507:
	s_add_i32 s35, s23, 0x18000
	s_or_b32 s16, s50, 0x80
	s_mov_b32 s10, s74
	s_mov_b32 s11, s75
	s_mov_b32 m0, s35
	s_add_i32 s36, s23, 0x1a000
	s_waitcnt vmcnt(4)
	s_barrier
	buffer_load_dwordx4 v151, s[8:11], s16 offen lds
	s_mov_b32 m0, s36
	s_add_i32 s37, s23, 0x8000
	buffer_load_dwordx4 v153, s[8:11], s16 offen lds
	s_or_b32 s16, s49, 0x80
	s_mov_b32 m0, s37
	s_add_i32 s38, s23, 0xa000
	buffer_load_dwordx4 v150, s[72:75], s16 offen lds
	s_mov_b32 m0, s38
	s_add_i32 s39, s23, 0x1c000
	buffer_load_dwordx4 v152, s[72:75], s16 offen lds
	s_or_b32 s16, s50, 0x80080
	s_mov_b32 m0, s39
	s_add_i32 s40, s23, 0x1e000
	buffer_load_dwordx4 v151, s[8:11], s16 offen lds
	s_mov_b32 m0, s40
	v_and_b32_e32 v1, 15, v0
	buffer_load_dwordx4 v153, s[8:11], s16 offen lds
	v_and_b32_e32 v2, 48, v0
	v_lshlrev_b32_e32 v0, 2, v0
	v_lshl_or_b32 v1, v1, 6, v2
	s_lshl_b32 s10, s14, 13
	v_and_b32_e32 v0, 32, v0
	v_bitop3_b32 v2, v1, s10, v0 bitop3:0xde
	s_lshl_b32 s10, s15, 12
	s_and_b32 s10, s10, 0x3000
	s_add_i32 s11, 0, 0x10000
	s_waitcnt vmcnt(10)
	s_add_i32 s41, s23, 0xc000
	s_add_i32 s42, s23, 0xe000
	v_xad_u32 v0, v1, v0, s11
	s_add_u32 s43, s4, 0xf8000000
	s_addc_u32 s44, s5, -1
	s_mov_b32 s45, 0
	v_add_u32_e32 v154, s10, v0
	v_add_u32_e32 v155, 0, v2
	s_barrier

.LBB0_1632:
	s_add_u32 s12, s4, 0x5900000
	s_addc_u32 s13, s5, 0
	s_add_i32 s26, s2, 0x18000
	s_or_b32 s4, s42, 0x80
	s_mov_b32 s10, s74
	s_mov_b32 s11, s75
	s_mov_b32 m0, s26
	s_add_i32 s27, s2, 0x1a000
	s_waitcnt vmcnt(4)
	s_barrier
	buffer_load_dwordx4 v130, s[8:11], s4 offen lds
	s_mov_b32 m0, s27
	s_add_i32 s28, s2, 0x8000
	buffer_load_dwordx4 v131, s[8:11], s4 offen lds
	s_or_b32 s4, s41, 0x80
	s_mov_b32 m0, s28
	s_add_i32 s29, s2, 0xa000
	buffer_load_dwordx4 v130, s[72:75], s4 offen lds
	s_mov_b32 m0, s29
	s_add_i32 s30, s2, 0x1c000
	buffer_load_dwordx4 v131, s[72:75], s4 offen lds
	s_or_b32 s4, s42, 0x80080
	s_mov_b32 m0, s30
	s_add_i32 s31, s2, 0x1e000
	buffer_load_dwordx4 v130, s[8:11], s4 offen lds
	s_mov_b32 m0, s31
	v_and_b32_e32 v1, 15, v0
	buffer_load_dwordx4 v131, s[8:11], s4 offen lds
	v_and_b32_e32 v2, 48, v0
	v_lshlrev_b32_e32 v0, 2, v0
	v_lshl_or_b32 v1, v1, 6, v2
	s_lshl_b32 s4, s14, 13
	v_and_b32_e32 v0, 32, v0
	v_bitop3_b32 v2, v1, s4, v0 bitop3:0xde
	s_lshl_b32 s4, s15, 12
	s_add_i32 s5, 0, 0x10000
	s_waitcnt vmcnt(10)
	s_and_b32 s4, s4, 0x3000
	v_xad_u32 v0, v1, v0, s5
	s_add_i32 s35, s2, 0xc000
	s_add_i32 s36, s2, 0xe000
	s_mov_b32 s38, 0
	v_add_u32_e32 v132, s4, v0
	v_add_u32_e32 v133, 0, v2
	s_barrier
	s_waitcnt vmcnt(10)
